# prologue expert conversion: touch loads per 32-byte sector of the wave's next row behind the row's own loads
# speedup vs baseline: 1.0006x; 1.0006x over previous
.LBB0_41:
	s_add_i32 s23, s22, 0xffffc000
	s_cmpk_gt_i32 s22, 0x3fff
	v_readlane_b32 s48, v253, 58
	s_cselect_b64 s[44:45], -1, 0
	v_readlane_b32 s49, v253, 59
	v_readlane_b32 s50, v253, 60
	v_readlane_b32 s51, v253, 61
	v_readlane_b32 s60, v254, 6
	v_readlane_b32 s61, v254, 7
	s_and_b64 s[24:25], s[44:45], exec
	v_readlane_b32 s62, v254, 8
	v_readlane_b32 s63, v254, 9
	s_mov_b64 s[48:49], s[60:61]
	s_cselect_b32 s24, s23, s22
	s_mov_b64 s[50:51], s[62:63]
	s_mov_b32 s23, 0x12b00000
	s_cselect_b32 s26, s51, s49
	s_cselect_b32 s27, s50, s48
	s_cselect_b32 s23, s23, 0xab00000
	s_add_i32 s86, s24, s16
	s_ashr_i32 s87, s86, 31
	s_lshl_b64 s[24:25], s[86:87], 13
	s_add_u32 s24, s27, s24
	s_addc_u32 s25, s26, s25
	s_add_i32 s100, s22, s20
	s_xor_b32 s101, s100, s22
	s_lshr_b32 s101, s101, 14
	s_cmp_eq_u32 s101, 0
	s_cselect_b32 s100, s20, 0
	s_lshl_b32 s100, s100, 13
	s_add_u32 s100, s24, s100
	s_addc_u32 s101, s25, 0
	v_lshl_add_u64 v[130:131], v[22:23], 4, s[100:101]
	s_add_u32 s100, s100, 0x1000
	s_addc_u32 s101, s101, 0
	v_lshl_add_u64 v[134:135], v[22:23], 4, s[100:101]
	v_lshl_add_u64 v[62:63], v[22:23], 2, s[24:25]
	s_movk_i32 s24, 0x1000
	global_load_dwordx4 v[2:5], v[62:63], off nt
	global_load_dwordx4 v[6:9], v[62:63], off offset:1024 nt
	global_load_dwordx4 v[10:13], v[62:63], off offset:2048 nt
	global_load_dwordx4 v[14:17], v[62:63], off offset:3072 nt
	v_add_co_u32_e32 v86, vcc, s24, v62
	s_add_u32 s23, s10, s23
	s_nop 0
	v_addc_co_u32_e32 v87, vcc, 0, v63, vcc
	global_load_dwordx4 v[62:65], v[86:87], off nt
	global_load_dwordx4 v[66:69], v[86:87], off offset:1024 nt
	global_load_dwordx4 v[82:85], v[86:87], off offset:2048 nt
	s_nop 0
	global_load_dwordx4 v[86:89], v[86:87], off offset:3072 nt
	global_load_dword v132, v[130:131], off
	global_load_dword v132, v[130:131], off offset:32
	global_load_dword v132, v[134:135], off
	global_load_dword v132, v[134:135], off offset:32
	v_readlane_b32 s52, v253, 62
	v_readlane_b32 s53, v253, 63
	v_readlane_b32 s54, v254, 0
	v_readlane_b32 s55, v254, 1
	v_readlane_b32 s56, v254, 2
	v_readlane_b32 s57, v254, 3
	v_readlane_b32 s58, v254, 4
	v_readlane_b32 s59, v254, 5
	s_waitcnt vmcnt(11)
	v_max_f32_e64 v55, |v5|, |v5|
	v_max_f32_e64 v57, |v4|, |v4|
	s_waitcnt vmcnt(10)
	v_max_f32_e64 v61, |v9|, |v9|
	v_max_f32_e64 v70, |v8|, |v8|
	s_waitcnt vmcnt(9)
	v_max_f32_e64 v72, |v13|, |v13|
	v_max_f32_e64 v74, |v12|, |v12|
	s_waitcnt vmcnt(8)
	v_max_f32_e64 v81, |v17|, |v17|
	v_max_f32_e64 v90, |v16|, |v16|
	v_max_f32_e32 v55, v57, v55
	v_max_f32_e32 v57, v70, v61
	v_max_f32_e32 v61, v74, v72
	v_max_f32_e32 v70, v90, v81
	s_waitcnt vmcnt(7)
	v_max_f32_e64 v72, |v65|, |v65|
	v_max_f32_e64 v74, |v64|, |v64|
	s_waitcnt vmcnt(6)
	v_max_f32_e64 v81, |v69|, |v69|
	v_max_f32_e64 v90, |v68|, |v68|
	v_max3_f32 v55, |v2|, |v3|, v55
	v_max3_f32 v57, |v6|, |v7|, v57
	s_waitcnt vmcnt(5)
	v_max_f32_e64 v91, |v85|, |v85|
	v_max_f32_e64 v92, |v84|, |v84|
	s_waitcnt vmcnt(4)
	v_max_f32_e64 v93, |v89|, |v89|
	v_max_f32_e64 v94, |v88|, |v88|
	v_max3_f32 v61, |v10|, |v11|, v61
	v_max3_f32 v70, |v14|, |v15|, v70
	v_max_f32_e32 v72, v74, v72
	v_max_f32_e32 v74, v90, v81
	v_max3_f32 v55, v55, 0, v57
	v_max_f32_e32 v81, v92, v91
	v_max_f32_e32 v90, v94, v93
	v_max3_f32 v57, |v62|, |v63|, v72
	v_max3_f32 v72, |v66|, |v67|, v74
	v_max3_f32 v55, v55, v61, v70
	v_max3_f32 v74, |v82|, |v83|, v81
	v_max3_f32 v81, |v86|, |v87|, v90
	v_max3_f32 v55, v55, v57, v72
	v_max3_f32 v55, v55, v74, v81
	s_nop 1
	v_mov_b32_dpp v57, v55 quad_perm:[1,0,3,2] row_mask:0xf bank_mask:0xf bound_ctrl:1
	v_max_f32_e32 v57, v57, v57
	v_max_f32_e32 v55, v55, v57
	s_nop 1
	v_mov_b32_dpp v57, v55 quad_perm:[2,3,0,1] row_mask:0xf bank_mask:0xf bound_ctrl:1
	v_max_f32_e32 v57, v57, v57
	v_max_f32_e32 v55, v55, v57
	s_nop 1
	v_mov_b32_dpp v57, v55 row_half_mirror row_mask:0xf bank_mask:0xf bound_ctrl:1
	v_max_f32_e32 v57, v57, v57
	v_max_f32_e32 v55, v55, v57
	s_nop 1
	v_mov_b32_dpp v57, v55 row_mirror row_mask:0xf bank_mask:0xf bound_ctrl:1
	v_max_f32_e32 v57, v57, v57
	v_max_f32_e32 v55, v55, v57
	s_nop 0
	v_readlane_b32 s26, v55, 32
	v_readlane_b32 s27, v55, 48
	v_readlane_b32 s24, v55, 0
	v_readlane_b32 s25, v55, 16
	v_max_f32_e64 v55, s27, s27
	v_max_f32_e64 v57, s26, s26
	v_mov_b32_e32 v61, s25
	v_max_f32_e32 v55, v57, v55
	v_max3_f32 v55, s24, v61, v55
	v_mul_f32_e32 v57, 0x3e088889, v55
	v_cmp_lt_f32_e32 vcc, 0, v55
	s_mul_hi_i32 s26, s86, 0x600
	s_nop 0
	v_cndmask_b32_e32 v55, 1.0, v57, vcc
	v_div_scale_f32 v57, s[24:25], v55, v55, 1.0
	v_rcp_f32_e32 v61, v57
	v_div_scale_f32 v70, vcc, 1.0, v55, 1.0
	s_addc_u32 s25, s11, 0
	v_fma_f32 v72, -v57, v61, 1.0
	v_fmac_f32_e32 v61, v72, v61
	v_mul_f32_e32 v72, v70, v61
	v_fma_f32 v74, -v57, v72, v70
	v_fmac_f32_e32 v72, v74, v61
	v_fma_f32 v57, -v57, v72, v70
	v_div_fmas_f32 v57, v57, v61, v72
	v_div_fixup_f32 v70, v57, v55, 1.0
	s_mul_i32 s24, s86, 0x600
	v_pk_mul_f32 v[2:3], v[2:3], v[70:71] op_sel_hi:[1,0]
	v_pk_mul_f32 v[4:5], v[4:5], v[70:71] op_sel_hi:[1,0]
	v_pk_mul_f32 v[6:7], v[6:7], v[70:71] op_sel_hi:[1,0]
	v_pk_mul_f32 v[8:9], v[8:9], v[70:71] op_sel_hi:[1,0]
	v_pk_mul_f32 v[10:11], v[10:11], v[70:71] op_sel_hi:[1,0]
	v_pk_mul_f32 v[12:13], v[12:13], v[70:71] op_sel_hi:[1,0]
	v_pk_mul_f32 v[14:15], v[14:15], v[70:71] op_sel_hi:[1,0]
	v_pk_mul_f32 v[16:17], v[16:17], v[70:71] op_sel_hi:[1,0]
	v_pk_mul_f32 v[62:63], v[62:63], v[70:71] op_sel_hi:[1,0]
	v_pk_mul_f32 v[64:65], v[64:65], v[70:71] op_sel_hi:[1,0]
	v_pk_mul_f32 v[66:67], v[66:67], v[70:71] op_sel_hi:[1,0]
	v_pk_mul_f32 v[68:69], v[68:69], v[70:71] op_sel_hi:[1,0]
	v_pk_mul_f32 v[82:83], v[82:83], v[70:71] op_sel_hi:[1,0]
	v_pk_mul_f32 v[84:85], v[84:85], v[70:71] op_sel_hi:[1,0]
	v_pk_mul_f32 v[86:87], v[86:87], v[70:71] op_sel_hi:[1,0]
	v_pk_mul_f32 v[88:89], v[88:89], v[70:71] op_sel_hi:[1,0]
	s_add_u32 s24, s23, s24
	v_cvt_pk_bf16_f32 v2, v2, v3
	v_cvt_pk_bf16_f32 v3, v4, v5
	v_cvt_pk_bf16_f32 v4, v6, v7
	v_cvt_pk_bf16_f32 v5, v8, v9
	v_cvt_pk_bf16_f32 v6, v10, v11
	v_cvt_pk_bf16_f32 v7, v12, v13
	v_cvt_pk_bf16_f32 v8, v14, v15
	v_cvt_pk_bf16_f32 v9, v16, v17
	v_cvt_pk_bf16_f32 v10, v62, v63
	v_cvt_pk_bf16_f32 v11, v64, v65
	v_cvt_pk_bf16_f32 v12, v66, v67
	v_cvt_pk_bf16_f32 v13, v68, v69
	v_cvt_pk_bf16_f32 v14, v82, v83
	v_cvt_pk_bf16_f32 v15, v84, v85
	v_cvt_pk_bf16_f32 v16, v86, v87
	v_cvt_pk_bf16_f32 v17, v88, v89
	s_addc_u32 s25, s25, s26
	v_cvt_scalef32_pk32_fp6_bf16 v[62:67], v[2:17], 1.0
	v_lshl_add_u64 v[2:3], s[24:25], 0, v[44:45]
	global_store_dwordx4 v[2:3], v[62:65], off
	v_lshl_add_u64 v[2:3], s[24:25], 0, v[30:31]
	global_store_dwordx2 v[2:3], v[66:67], off offset:1024
	s_and_saveexec_b64 s[68:69], s[2:3]
	s_cbranch_execz .LBB0_40
	s_and_b64 s[24:25], s[44:45], exec
	s_mov_b32 s23, 0x1ac00000
	s_cselect_b32 s23, s23, 0x1ab00000
	s_add_u32 s23, s10, s23
	s_addc_u32 s26, s11, 0
	s_lshl_b64 s[24:25], s[86:87], 2
	s_add_u32 s24, s23, s24
	s_addc_u32 s25, s26, s25
	global_store_dword v18, v55, s[24:25]
	s_branch .LBB0_40
